# adds: P2 low-rank gate column loop (fragments from global): 6 of 8 k-steps requested up front, counted waits
# baseline (speedup 1.0000x reference)
; template <int NB, class AR, class BR, class EP>
; __device__ __forceinline__ void wave_gemm32(const AR& arow, const BR& brow, const EP& epi, int K, int lane) {
;     ...
;     for (int k = 0; k < K; k += 32) {
;         bf16x8 af[2], bfr[NB][2];
; #pragma unroll
;         for (int m = 0; m < 2; ++m) af[m] = *(const bf16x8*)(a[m] + k);
; #pragma unroll
;         for (int w = 0; w < NB; ++w)
; #pragma unroll
;             for (int n = 0; n < 2; ++n) bfr[w][n] = *(const bf16x8*)(b[w][n] + k);
; #pragma unroll
;         for (int w = 0; w < NB; ++w)
; #pragma unroll
;             for (int m = 0; m < 2; ++m)
; #pragma unroll
;                 for (int n = 0; n < 2; ++n) acc[w][m][n] = __builtin_amdgcn_mfma_f32_16x16x32_bf16(af[m], bfr[w][n], acc[w][m][n], 0, 0, 0);
;     }
.LBB0_203:
	s_waitcnt vmcnt(0)
	v_lshl_add_u64 v[56:57], v[18:19], 0, s[0:1]
	v_lshl_add_u64 v[52:53], v[20:21], 0, s[0:1]
	v_lshl_add_u64 v[54:55], v[22:23], 0, s[0:1]
	v_add_co_u32_e32 v58, vcc, s15, v56
	s_nop 1
	v_addc_co_u32_e32 v59, vcc, 0, v57, vcc
	v_add_co_u32_e32 v56, vcc, s14, v56
	s_nop 1
	v_addc_co_u32_e32 v57, vcc, 0, v57, vcc
	global_load_dwordx4 v[24:27], v[52:53], off offset:-256
	global_load_dwordx4 v[28:31], v[54:55], off offset:-256
	global_load_dwordx4 v[32:35], v[56:57], off offset:0
	global_load_dwordx4 v[36:39], v[58:59], off offset:0
	global_load_dwordx4 v[40:43], v[52:53], off offset:-192
	global_load_dwordx4 v[44:47], v[54:55], off offset:-192
	global_load_dwordx4 v[48:51], v[56:57], off offset:64
	global_load_dwordx4 v[60:63], v[58:59], off offset:64
	global_load_dwordx4 v[64:67], v[52:53], off offset:-128
	global_load_dwordx4 v[68:71], v[54:55], off offset:-128
	global_load_dwordx4 v[72:75], v[56:57], off offset:128
	global_load_dwordx4 v[76:79], v[58:59], off offset:128
	global_load_dwordx4 v[80:83], v[52:53], off offset:-64
	global_load_dwordx4 v[84:87], v[54:55], off offset:-64
	global_load_dwordx4 v[88:91], v[56:57], off offset:192
	global_load_dwordx4 v[92:95], v[58:59], off offset:192
	global_load_dwordx4 v[96:99], v[52:53], off offset:0
	global_load_dwordx4 v[100:103], v[54:55], off offset:0
	global_load_dwordx4 v[104:107], v[56:57], off offset:256
	global_load_dwordx4 v[108:111], v[58:59], off offset:256
	global_load_dwordx4 v[112:115], v[52:53], off offset:64
	global_load_dwordx4 v[116:119], v[54:55], off offset:64
	global_load_dwordx4 v[120:123], v[56:57], off offset:320
	global_load_dwordx4 v[124:127], v[58:59], off offset:320
	s_waitcnt vmcnt(20)
	v_mfma_f32_16x16x32_bf16 v[14:17], v[24:27], v[32:35], v[14:17]
	v_mfma_f32_16x16x32_bf16 v[10:13], v[24:27], v[36:39], v[10:13]
	v_mfma_f32_16x16x32_bf16 v[6:9], v[28:31], v[32:35], v[6:9]
	v_mfma_f32_16x16x32_bf16 v[2:5], v[28:31], v[36:39], v[2:5]
	global_load_dwordx4 v[24:27], v[52:53], off offset:128
	global_load_dwordx4 v[28:31], v[54:55], off offset:128
	global_load_dwordx4 v[32:35], v[56:57], off offset:384
	global_load_dwordx4 v[36:39], v[58:59], off offset:384
	s_waitcnt vmcnt(20)
	v_mfma_f32_16x16x32_bf16 v[14:17], v[40:43], v[48:51], v[14:17]
	v_mfma_f32_16x16x32_bf16 v[10:13], v[40:43], v[60:63], v[10:13]
	v_mfma_f32_16x16x32_bf16 v[6:9], v[44:47], v[48:51], v[6:9]
	v_mfma_f32_16x16x32_bf16 v[2:5], v[44:47], v[60:63], v[2:5]
	global_load_dwordx4 v[40:43], v[52:53], off offset:192
	global_load_dwordx4 v[44:47], v[54:55], off offset:192
	global_load_dwordx4 v[48:51], v[56:57], off offset:448
	global_load_dwordx4 v[60:63], v[58:59], off offset:448
	s_waitcnt vmcnt(20)
	v_mfma_f32_16x16x32_bf16 v[14:17], v[64:67], v[72:75], v[14:17]
	v_mfma_f32_16x16x32_bf16 v[10:13], v[64:67], v[76:79], v[10:13]
	v_mfma_f32_16x16x32_bf16 v[6:9], v[68:71], v[72:75], v[6:9]
	v_mfma_f32_16x16x32_bf16 v[2:5], v[68:71], v[76:79], v[2:5]
	s_waitcnt vmcnt(16)
	v_mfma_f32_16x16x32_bf16 v[14:17], v[80:83], v[88:91], v[14:17]
	v_mfma_f32_16x16x32_bf16 v[10:13], v[80:83], v[92:95], v[10:13]
	v_mfma_f32_16x16x32_bf16 v[6:9], v[84:87], v[88:91], v[6:9]
	v_mfma_f32_16x16x32_bf16 v[2:5], v[84:87], v[92:95], v[2:5]
	s_waitcnt vmcnt(12)
	v_mfma_f32_16x16x32_bf16 v[14:17], v[96:99], v[104:107], v[14:17]
	v_mfma_f32_16x16x32_bf16 v[10:13], v[96:99], v[108:111], v[10:13]
	v_mfma_f32_16x16x32_bf16 v[6:9], v[100:103], v[104:107], v[6:9]
	v_mfma_f32_16x16x32_bf16 v[2:5], v[100:103], v[108:111], v[2:5]
	s_waitcnt vmcnt(8)
	v_mfma_f32_16x16x32_bf16 v[14:17], v[112:115], v[120:123], v[14:17]
	v_mfma_f32_16x16x32_bf16 v[10:13], v[112:115], v[124:127], v[10:13]
	v_mfma_f32_16x16x32_bf16 v[6:9], v[116:119], v[120:123], v[6:9]
	v_mfma_f32_16x16x32_bf16 v[2:5], v[116:119], v[124:127], v[2:5]
	s_waitcnt vmcnt(4)
	v_mfma_f32_16x16x32_bf16 v[14:17], v[24:27], v[32:35], v[14:17]
	v_mfma_f32_16x16x32_bf16 v[10:13], v[24:27], v[36:39], v[10:13]
	v_mfma_f32_16x16x32_bf16 v[6:9], v[28:31], v[32:35], v[6:9]
	v_mfma_f32_16x16x32_bf16 v[2:5], v[28:31], v[36:39], v[2:5]
	s_waitcnt vmcnt(0)
	v_mfma_f32_16x16x32_bf16 v[14:17], v[40:43], v[48:51], v[14:17]
	v_mfma_f32_16x16x32_bf16 v[10:13], v[40:43], v[60:63], v[10:13]
	v_mfma_f32_16x16x32_bf16 v[6:9], v[44:47], v[48:51], v[6:9]
	v_mfma_f32_16x16x32_bf16 v[2:5], v[44:47], v[60:63], v[2:5]
	v_lshl_add_u64 v[18:19], v[18:19], 0, s[4:5]
	v_lshl_add_u64 v[20:21], v[20:21], 0, s[4:5]
	v_lshl_add_u64 v[22:23], v[22:23], 0, s[4:5]
	s_addk_i32 s9, 0x100
	s_cmpk_lt_u32 s9, 0x3e0
	s_cbranch_scc1 .LBB0_203
	s_branch .LBB0_208

; template <int NB, class AR, class BR, class EP>
; __device__ __forceinline__ void wave_gemm32(const AR& arow, const BR& brow, const EP& epi, int K, int lane) {
;     ...
;     for (int k = 0; k < K; k += 32) {
;         bf16x8 af[2], bfr[NB][2];
; #pragma unroll
;         for (int m = 0; m < 2; ++m) af[m] = *(const bf16x8*)(a[m] + k);
; #pragma unroll
;         for (int w = 0; w < NB; ++w)
; #pragma unroll
;             for (int n = 0; n < 2; ++n) bfr[w][n] = *(const bf16x8*)(b[w][n] + k);
; #pragma unroll
;         for (int w = 0; w < NB; ++w)
; #pragma unroll
;             for (int m = 0; m < 2; ++m)
; #pragma unroll
;                 for (int n = 0; n < 2; ++n) acc[w][m][n] = __builtin_amdgcn_mfma_f32_16x16x32_bf16(af[m], bfr[w][n], acc[w][m][n], 0, 0, 0);
;     }
.LBB0_207:
	s_waitcnt vmcnt(0)
	v_lshl_add_u64 v[56:57], v[18:19], 0, s[0:1]
	v_lshl_add_u64 v[52:53], v[20:21], 0, s[0:1]
	v_lshl_add_u64 v[54:55], v[22:23], 0, s[0:1]
	v_add_co_u32_e32 v58, vcc, s9, v56
	s_nop 1
	v_addc_co_u32_e32 v59, vcc, 0, v57, vcc
	v_add_co_u32_e32 v56, vcc, s8, v56
	s_nop 1
	v_addc_co_u32_e32 v57, vcc, 0, v57, vcc
	global_load_dwordx4 v[24:27], v[52:53], off offset:-256
	global_load_dwordx4 v[28:31], v[54:55], off offset:-256
	global_load_dwordx4 v[32:35], v[56:57], off offset:0
	global_load_dwordx4 v[36:39], v[58:59], off offset:0
	global_load_dwordx4 v[40:43], v[52:53], off offset:-192
	global_load_dwordx4 v[44:47], v[54:55], off offset:-192
	global_load_dwordx4 v[48:51], v[56:57], off offset:64
	global_load_dwordx4 v[60:63], v[58:59], off offset:64
	global_load_dwordx4 v[64:67], v[52:53], off offset:-128
	global_load_dwordx4 v[68:71], v[54:55], off offset:-128
	global_load_dwordx4 v[72:75], v[56:57], off offset:128
	global_load_dwordx4 v[76:79], v[58:59], off offset:128
	global_load_dwordx4 v[80:83], v[52:53], off offset:-64
	global_load_dwordx4 v[84:87], v[54:55], off offset:-64
	global_load_dwordx4 v[88:91], v[56:57], off offset:192
	global_load_dwordx4 v[92:95], v[58:59], off offset:192
	global_load_dwordx4 v[96:99], v[52:53], off offset:0
	global_load_dwordx4 v[100:103], v[54:55], off offset:0
	global_load_dwordx4 v[104:107], v[56:57], off offset:256
	global_load_dwordx4 v[108:111], v[58:59], off offset:256
	global_load_dwordx4 v[112:115], v[52:53], off offset:64
	global_load_dwordx4 v[116:119], v[54:55], off offset:64
	global_load_dwordx4 v[120:123], v[56:57], off offset:320
	global_load_dwordx4 v[124:127], v[58:59], off offset:320
	s_waitcnt vmcnt(20)
	v_mfma_f32_16x16x32_bf16 v[14:17], v[24:27], v[32:35], v[14:17]
	v_mfma_f32_16x16x32_bf16 v[10:13], v[24:27], v[36:39], v[10:13]
	v_mfma_f32_16x16x32_bf16 v[6:9], v[28:31], v[32:35], v[6:9]
	v_mfma_f32_16x16x32_bf16 v[2:5], v[28:31], v[36:39], v[2:5]
	global_load_dwordx4 v[24:27], v[52:53], off offset:128
	global_load_dwordx4 v[28:31], v[54:55], off offset:128
	global_load_dwordx4 v[32:35], v[56:57], off offset:384
	global_load_dwordx4 v[36:39], v[58:59], off offset:384
	s_waitcnt vmcnt(20)
	v_mfma_f32_16x16x32_bf16 v[14:17], v[40:43], v[48:51], v[14:17]
	v_mfma_f32_16x16x32_bf16 v[10:13], v[40:43], v[60:63], v[10:13]
	v_mfma_f32_16x16x32_bf16 v[6:9], v[44:47], v[48:51], v[6:9]
	v_mfma_f32_16x16x32_bf16 v[2:5], v[44:47], v[60:63], v[2:5]
	global_load_dwordx4 v[40:43], v[52:53], off offset:192
	global_load_dwordx4 v[44:47], v[54:55], off offset:192
	global_load_dwordx4 v[48:51], v[56:57], off offset:448
	global_load_dwordx4 v[60:63], v[58:59], off offset:448
	s_waitcnt vmcnt(20)
	v_mfma_f32_16x16x32_bf16 v[14:17], v[64:67], v[72:75], v[14:17]
	v_mfma_f32_16x16x32_bf16 v[10:13], v[64:67], v[76:79], v[10:13]
	v_mfma_f32_16x16x32_bf16 v[6:9], v[68:71], v[72:75], v[6:9]
	v_mfma_f32_16x16x32_bf16 v[2:5], v[68:71], v[76:79], v[2:5]
	s_waitcnt vmcnt(16)
	v_mfma_f32_16x16x32_bf16 v[14:17], v[80:83], v[88:91], v[14:17]
	v_mfma_f32_16x16x32_bf16 v[10:13], v[80:83], v[92:95], v[10:13]
	v_mfma_f32_16x16x32_bf16 v[6:9], v[84:87], v[88:91], v[6:9]
	v_mfma_f32_16x16x32_bf16 v[2:5], v[84:87], v[92:95], v[2:5]
	s_waitcnt vmcnt(12)
	v_mfma_f32_16x16x32_bf16 v[14:17], v[96:99], v[104:107], v[14:17]
	v_mfma_f32_16x16x32_bf16 v[10:13], v[96:99], v[108:111], v[10:13]
	v_mfma_f32_16x16x32_bf16 v[6:9], v[100:103], v[104:107], v[6:9]
	v_mfma_f32_16x16x32_bf16 v[2:5], v[100:103], v[108:111], v[2:5]
	s_waitcnt vmcnt(8)
	v_mfma_f32_16x16x32_bf16 v[14:17], v[112:115], v[120:123], v[14:17]
	v_mfma_f32_16x16x32_bf16 v[10:13], v[112:115], v[124:127], v[10:13]
	v_mfma_f32_16x16x32_bf16 v[6:9], v[116:119], v[120:123], v[6:9]
	v_mfma_f32_16x16x32_bf16 v[2:5], v[116:119], v[124:127], v[2:5]
	s_waitcnt vmcnt(4)
	v_mfma_f32_16x16x32_bf16 v[14:17], v[24:27], v[32:35], v[14:17]
	v_mfma_f32_16x16x32_bf16 v[10:13], v[24:27], v[36:39], v[10:13]
	v_mfma_f32_16x16x32_bf16 v[6:9], v[28:31], v[32:35], v[6:9]
	v_mfma_f32_16x16x32_bf16 v[2:5], v[28:31], v[36:39], v[2:5]
	s_waitcnt vmcnt(0)
	v_mfma_f32_16x16x32_bf16 v[14:17], v[40:43], v[48:51], v[14:17]
	v_mfma_f32_16x16x32_bf16 v[10:13], v[40:43], v[60:63], v[10:13]
	v_mfma_f32_16x16x32_bf16 v[6:9], v[44:47], v[48:51], v[6:9]
	v_mfma_f32_16x16x32_bf16 v[2:5], v[44:47], v[60:63], v[2:5]
	v_lshl_add_u64 v[18:19], v[18:19], 0, s[4:5]
	v_lshl_add_u64 v[20:21], v[20:21], 0, s[4:5]
	v_lshl_add_u64 v[22:23], v[22:23], 0, s[4:5]
	s_addk_i32 s7, 0x100
	s_cmpk_gt_u32 s7, 0x1df
	s_cbranch_scc0 .LBB0_207
